# baseline (speedup 1.0000x reference)
.Llin_skip:
	s_mov_b64 exec, s[58:59]
	s_nop 4
	v_add_f32_dpp v40, v40, v40 quad_perm:[1,0,3,2] row_mask:0xf bank_mask:0xf
	v_add_f32_dpp v41, v41, v41 quad_perm:[1,0,3,2] row_mask:0xf bank_mask:0xf
	s_nop 1
	v_add_f32_dpp v40, v40, v40 quad_perm:[2,3,0,1] row_mask:0xf bank_mask:0xf
	v_add_f32_dpp v41, v41, v41 quad_perm:[2,3,0,1] row_mask:0xf bank_mask:0xf
	v_cmp_eq_u32_e32 vcc, 0, v99
	s_movk_i32 s45, 0xe0
	v_cmp_gt_u32_e64 s[60:61], s45, v98
	v_add_u32_e32 v12, 0x38000000, v101
	v_cvt_f32_u32_e32 v48, v96
	s_and_b64 vcc, vcc, s[60:61]
	s_and_saveexec_b64 s[60:61], vcc
	v_mov_b32_e32 v49, v100
	v_mul_f32_e32 v12, v12, v20
	v_mul_f32_e32 v46, v40, v100
	v_mul_f32_e32 v47, v41, v100
	v_mul_f32_e32 v48, v48, v100
	v_lshlrev_b32_e32 v13, 4, v98
	v_add_u32_e32 v13, 0x23360, v13
	ds_write_b128 v13, v[46:49]
	v_lshlrev_b32_e32 v13, 2, v98
	v_add_u32_e32 v13, 0x22200, v13
	ds_write_b32 v13, v12
	s_mov_b64 exec, s[60:61]
	s_waitcnt lgkmcnt(0)
	s_barrier
	v_mov_b32_e32 v11, 0x24860
	ds_read_b64 v[12:13], v11
	v_mov_b32_e32 v62, 0x23360
	v_mov_b32_e32 v2, v55
	s_waitcnt lgkmcnt(0)
	v_readfirstlane_b32 s62, v12
	v_readfirstlane_b32 s63, v13
	s_add_i32 s62, s62, 1
	s_lshr_b32 s62, s62, 1
	s_add_i32 s63, s63, 1
	s_lshr_b32 s63, s63, 1
	s_mov_b64 exec, 1
	ds_add_rtn_u32 v10, v59, v60
	s_mov_b64 exec, -1
	s_waitcnt lgkmcnt(0)
	v_readfirstlane_b32 s34, v10
	s_cmp_lt_u32 s34, s62
	s_cselect_b32 s45, s64, s65
	s_cselect_b32 s46, 0, s62
	s_cselect_b32 s48, s62, s63
	s_sub_u32 s47, s34, s46
	s_cmp_ge_u32 s47, s48
	s_cselect_b32 s52, 1, 0
	s_lshl_b32 s47, s47, 3
	s_add_u32 s45, s45, s47
	v_mov_b32_e32 v11, s45
	ds_read2_b32 v[12:13], v11 offset1:1
	s_waitcnt lgkmcnt(0)
	s_branch .Lp_top
.Lp_next:
	s_waitcnt lgkmcnt(8)
.Lp_top:
	s_cmp_eq_u32 s52, 1
	s_cbranch_scc1 .Lp_done
	v_readfirstlane_b32 s35, v12
	v_readfirstlane_b32 s36, v13
	s_nop 1
	v_mov_b32_e32 v11, s35
	v_mov_b32_e32 v14, s36
	v_cndmask_b32_e64 v12, v11, v14, s[54:55]
	v_cndmask_b32_e64 v13, v11, v14, s[56:57]
	v_lshl_add_u32 v12, v12, 3, v61
	v_lshl_add_u32 v14, v13, 4, v62
	ds_read_b64 v[2:3], v12
	ds_read_b128 v[4:7], v14
	s_mov_b64 exec, 1
	ds_add_rtn_u32 v10, v59, v60
	s_mov_b64 exec, -1
	v_mad_u32_u24 v9, v13, s49, v58
	v_mov_b32_e32 v8, v56
	s_waitcnt lgkmcnt(1)
	v_add_u32_e32 v2, v2, v55
	v_and_b32_e32 v3, v3, v63
	s_nop 0
	v_readlane_b32 s41, v3, 0
	v_readlane_b32 s42, v3, 4
	s_max_u32 s43, s41, s42
	s_cmp_eq_u32 s43, 0
	s_cbranch_scc1 .Lp_zero
	ds_read_b64 v[36:37], v2
	v_cmp_gt_u32_e32 vcc, v3, v8
	v_add_u32_e32 v2, 64, v2
	v_add_u32_e32 v8, 16, v8
	v_mov_b32_e32 v33, 0x3c00
	s_waitcnt lgkmcnt(0)
	v_perm_b32 v32, v37, v36, v57
	v_cndmask_b32_e32 v33, 0, v33, vcc
	s_nop 0
	v_cndmask_b32_e32 v32, 0, v32, vcc
	s_nop 1
	v_mfma_f32_32x32x16_f16 v[96:111], v[32:35], v[64:67], 0
	v_mfma_f32_32x32x16_f16 v[112:127], v[32:35], v[68:71], 0
	v_readfirstlane_b32 s34, v10
	s_cmp_lt_u32 s34, s62
	s_cselect_b32 s45, s64, s65
	s_cselect_b32 s46, 0, s62
	s_cselect_b32 s48, s62, s63
	s_sub_u32 s47, s34, s46
	s_cmp_ge_u32 s47, s48
	s_cselect_b32 s52, 1, 0
	s_lshl_b32 s47, s47, 3
	s_add_u32 s45, s45, s47
	v_mov_b32_e32 v11, s45
	ds_read2_b32 v[12:13], v11 offset1:1
	s_mov_b32 s45, s43
	s_min_u32 s46, s45, 16
	s_add_i32 s46, s46, 3
	s_lshr_b32 s46, s46, 2
	s_cmp_eq_u32 s46, 4
	s_cbranch_scc1 .Lf4
	s_cmp_eq_u32 s46, 3
	s_cbranch_scc1 .Lf3
	s_cmp_eq_u32 s46, 2
	s_cbranch_scc1 .Lf2

.Lp_zero:
	s_waitcnt lgkmcnt(0)
	v_readfirstlane_b32 s34, v10
	s_cmp_lt_u32 s34, s62
	s_cselect_b32 s45, s64, s65
	s_cselect_b32 s46, 0, s62
	s_cselect_b32 s48, s62, s63
	s_sub_u32 s47, s34, s46
	s_cmp_ge_u32 s47, s48
	s_cselect_b32 s52, 1, 0
	s_lshl_b32 s47, s47, 3
	s_add_u32 s45, s45, s47
	v_mov_b32_e32 v11, s45
	ds_read2_b32 v[12:13], v11 offset1:1
	v_mov_b32_e32 v24, 0
	v_mov_b32_e32 v25, 0
	v_mov_b32_e32 v26, 0
	v_mov_b32_e32 v27, 0
	v_mov_b32_e32 v28, 0
	v_mov_b32_e32 v29, 0
	v_mov_b32_e32 v30, 0
	v_mov_b32_e32 v31, 0
	s_branch .Lp_fin
.Lp_done:
	s_waitcnt lgkmcnt(0)
	v_xor_b32_e32 v102, 16, v18
	v_lshlrev_b32_e32 v102, 2, v102
	s_branch .LBB3_67
